# stack31 = stack23 + expert-phase gather: counted waits, each row chunk written to LDS as it arrives instead of one full wait
# baseline (speedup 1.0000x reference)
; DEVINL void phase5(const Params& P, unsigned char* smem) {
;     ...
;             for (int rp = 0; rp < 2; ++rp) {
;                 const int row = (t >> 3) + 64 * rp, r = rbeg + row;
;                 if (row < 80) {
;                     const bool ok = r < rend;
;                     const int tok = ok ? ctok[cls * NT + r] : 0; const f32x2 w2 = ok ? cw[cls * NT + r] : (f32x2){0.f, 0.f};
;                     if ((t & 7) == 0) { s_tok[row] = ok ? tok : -1; s_wl[row] = w2.x; s_wh[row] = w2.y; }
;                     const unsigned char* src = H2 + (size_t)tok * DM;
; #pragma unroll
;                     for (int i = 0; i < 8; ++i) { const int c = (t & 7) + 8 * i; *(u32x4*)(smem + row * 1024 + ((c ^ (row & 15)) << 4)) = *(const u32x4*)(src + c * 16); }
;                 }
.Lp5_g_norows1:
	v_cndmask_b32_e64 v141, -1, v54, s[82:83]
	v_cndmask_b32_e64 v142, -1, v55, s[86:87]
	s_cmp_lt_u32 s95, 16
	s_cbranch_scc1 .Lp5_g_w16
	s_waitcnt vmcnt(7)
	ds_write_b128 v131, v[66:69]
	s_waitcnt vmcnt(6)
	ds_write_b128 v132, v[70:73]
	s_waitcnt vmcnt(5)
	ds_write_b128 v133, v[74:77]
	s_waitcnt vmcnt(4)
	ds_write_b128 v134, v[78:81]
	s_waitcnt vmcnt(3)
	ds_write_b128 v135, v[82:85]
	s_waitcnt vmcnt(2)
	ds_write_b128 v136, v[86:89]
	s_waitcnt vmcnt(1)
	ds_write_b128 v137, v[90:93]
	s_waitcnt vmcnt(0)
	ds_write_b128 v138, v[94:97]
	s_branch .Lp5_g_wdone
.Lp5_g_w16:
	s_waitcnt vmcnt(15)
	ds_write_b128 v131, v[66:69]
	s_waitcnt vmcnt(14)
	ds_write_b128 v132, v[70:73]
	s_waitcnt vmcnt(13)
	ds_write_b128 v133, v[74:77]
	s_waitcnt vmcnt(12)
	ds_write_b128 v134, v[78:81]
	s_waitcnt vmcnt(11)
	ds_write_b128 v135, v[82:85]
	s_waitcnt vmcnt(10)
	ds_write_b128 v136, v[86:89]
	s_waitcnt vmcnt(9)
	ds_write_b128 v137, v[90:93]
	s_waitcnt vmcnt(8)
	ds_write_b128 v138, v[94:97]
.Lp5_g_wdone:
	v_cndmask_b32_e64 v56, 0, v56, s[82:83]
	v_cndmask_b32_e64 v57, 0, v57, s[82:83]
	v_cndmask_b32_e64 v58, 0, v58, s[86:87]
	v_cndmask_b32_e64 v59, 0, v59, s[86:87]
	s_mov_b64 s[82:83], exec
	s_and_b64 exec, s[82:83], s[90:91]
	v_add_u32_e32 v143, 0x24900, v140
	v_add_u32_e32 v144, 0x24a40, v140
	v_add_u32_e32 v145, 0x24b80, v140
	ds_write_b32 v143, v141
	ds_write_b32 v144, v56
	ds_write_b32 v145, v57
	s_and_b64 exec, exec, s[92:93]
	ds_write_b32 v143, v142 offset:256
	ds_write_b32 v144, v58 offset:256
	ds_write_b32 v145, v59 offset:256
	s_and_b64 exec, s[82:83], s[92:93]
	s_cbranch_execz .Lp5_g_skipw1
	v_add_u32_e32 v131, 0x10000, v131
	v_add_u32_e32 v132, 0x10000, v132
	v_add_u32_e32 v133, 0x10000, v133
	v_add_u32_e32 v134, 0x10000, v134
	v_add_u32_e32 v135, 0x10000, v135
	v_add_u32_e32 v136, 0x10000, v136
	v_add_u32_e32 v137, 0x10000, v137
	v_add_u32_e32 v138, 0x10000, v138
	s_waitcnt vmcnt(7)
	ds_write_b128 v131, v[98:101]
	s_waitcnt vmcnt(6)
	ds_write_b128 v132, v[102:105]
	s_waitcnt vmcnt(5)
	ds_write_b128 v133, v[106:109]
	s_waitcnt vmcnt(4)
	ds_write_b128 v134, v[110:113]
	s_waitcnt vmcnt(3)
	ds_write_b128 v135, v[114:117]
	s_waitcnt vmcnt(2)
	ds_write_b128 v136, v[118:121]
	s_waitcnt vmcnt(1)
	ds_write_b128 v137, v[122:125]
	s_waitcnt vmcnt(0)
	ds_write_b128 v138, v[126:129]
